# v23 + two map-1 Q fragments of the attention fast path kept in registers for the whole unit (2 fewer LDS reads per key tile)
# baseline (speedup 1.0000x reference)
.LBB0_639:
	s_ashr_i32 s18, s33, 7
	s_lshl_b32 s68, s18, 12
	s_lshl_b32 s4, s33, 8
	s_and_b32 s4, s4, 0xf00
	s_add_i32 s5, s68, s22
	s_add_i32 s16, s5, s4
	s_bfe_u32 s19, s33, 0x30004
	s_ashr_i32 s17, s16, 31
	s_mul_i32 s5, s16, 0x3200
	s_mul_hi_i32 s4, s16, 0x3200
	s_add_u32 s5, s20, s5
	s_addc_u32 s4, s21, s4
	s_lshl_b32 s65, s19, 8
	s_add_u32 s5, s5, s65
	s_addc_u32 s65, s4, 0
	s_add_u32 s4, s5, 0x1800
	s_addc_u32 s5, s65, 0
	v_xor_b32_e32 v6, 0x80, v164
	v_mov_b32_e32 v7, 0
	v_xor_b32_e32 v8, 0x80, v168
	v_mov_b32_e32 v9, 0
	v_lshl_add_u64 v[2:3], s[4:5], 0, v[162:163]
	s_mov_b32 m0, s24
	v_lshl_add_u64 v[4:5], v[2:3], 0, v[164:165]
	s_lshl_b32 s66, s18, 8
	global_load_lds_dwordx4 v[4:5], off
	v_lshl_add_u64 v[4:5], s[4:5], 0, v[166:167]
	v_lshl_add_u64 v[4:5], v[4:5], 0, v[168:169]
	s_mov_b32 m0, s35
	s_addk_i32 s66, 0x4000
	global_load_lds_dwordx4 v[4:5], off
	v_lshl_add_u64 v[4:5], v[2:3], 0, s[6:7]
	v_lshl_add_u64 v[4:5], v[4:5], 0, v[6:7]
	s_mov_b32 m0, s36
	s_lshl_b32 s65, s19, 7
	global_load_lds_dwordx4 v[4:5], off
	v_lshl_add_u64 v[4:5], s[4:5], 0, v[170:171]
	v_lshl_add_u64 v[4:5], v[4:5], 0, v[8:9]
	s_mov_b32 m0, s37
	v_mov_b32_e32 v12, v177
	global_load_lds_dwordx4 v[4:5], off
	v_lshl_add_u64 v[4:5], v[2:3], 0, s[8:9]
	v_lshl_add_u64 v[4:5], v[4:5], 0, v[164:165]
	s_mov_b32 m0, s38
	s_mov_b32 s70, 0
	global_load_lds_dwordx4 v[4:5], off
	v_lshl_add_u64 v[4:5], s[4:5], 0, v[172:173]
	v_lshl_add_u64 v[4:5], v[4:5], 0, v[168:169]
	s_mov_b32 m0, s39
	s_nop 0
	global_load_lds_dwordx4 v[4:5], off
	v_lshl_add_u64 v[4:5], v[2:3], 0, s[10:11]
	v_lshl_add_u64 v[4:5], v[4:5], 0, v[6:7]
	s_mov_b32 m0, s40
	s_nop 0
	global_load_lds_dwordx4 v[4:5], off
	v_lshl_add_u64 v[4:5], s[4:5], 0, v[174:175]
	v_lshl_add_u64 v[4:5], v[4:5], 0, v[8:9]
	s_mov_b32 m0, s41
	s_mul_i32 s4, s66, 0x3200
	global_load_lds_dwordx4 v[4:5], off
	v_mov_b32_e32 v2, v196
	s_mul_hi_i32 s5, s66, 0x3200
	v_ashrrev_i32_e32 v3, 4, v2
	s_add_u32 s4, s20, s4
	v_and_b32_e32 v4, 15, v2
	v_add_u32_e32 v8, s25, v3
	s_addc_u32 s5, s21, s5
	s_or_b32 s67, s65, 0x1000
	v_bitop3_b32 v9, v8, v4, 15 bitop3:0x6c
	v_mul_lo_u32 v8, v8, s44
	v_ashrrev_i32_e32 v5, 5, v2
	v_add_u32_e32 v8, s67, v8
	v_lshlrev_b32_e32 v9, 4, v9
	v_bfe_u32 v6, v2, 2, 3
	v_lshrrev_b32_e32 v7, 1, v2
	v_lshl_or_b32 v8, v8, 1, v9
	v_add_u32_e32 v9, s26, v5
	v_lshlrev_b32_e32 v7, 3, v2
	v_lshlrev_b32_e32 v10, 1, v9
	v_and_b32_e32 v7, 24, v7
	v_and_b32_e32 v10, 0xfffff0, v10
	v_and_b32_e32 v9, 4, v9
	v_lshlrev_b32_e32 v9, 1, v9
	v_and_b32_e32 v2, 0x60, v2
	v_or3_b32 v9, v9, v10, v6
	v_or3_b32 v2, s65, v2, v7
	v_mad_u32_u24 v2, v9, s44, v2
	s_mov_b32 m0, s54
	v_lshl_add_u32 v2, v2, 1, v198
	global_load_lds_dwordx4 v8, s[4:5]
	s_mov_b32 m0, s53
	s_mov_b32 s71, 64
	global_load_lds_dwordx4 v2, s[4:5]
	v_add_u32_e32 v2, s28, v3
	v_mul_lo_u32 v3, v2, s44
	v_bitop3_b32 v2, v2, v4, 15 bitop3:0x6c
	v_add_u32_e32 v3, s67, v3
	v_lshlrev_b32_e32 v2, 4, v2
	v_lshl_or_b32 v2, v3, 1, v2
	v_add_u32_e32 v3, s29, v5
	v_lshlrev_b32_e32 v4, 1, v3
	v_and_b32_e32 v5, 4, v3
	v_lshlrev_b32_e32 v5, 1, v5
	v_lshlrev_b32_e32 v3, 5, v3
	v_and_b32_e32 v4, 0xfffff0, v4
	v_and_b32_e32 v3, 0x60, v3
	v_or3_b32 v4, v5, v4, v6
	v_or3_b32 v3, v7, v3, s65
	v_mad_u32_u24 v3, v4, s44, v3
	s_mov_b32 m0, s64
	v_lshl_add_u32 v3, v3, 1, v198
	global_load_lds_dwordx4 v2, s[4:5]
	s_mov_b32 m0, s55
	v_mov_b32_e32 v2, v176
	global_load_lds_dwordx4 v3, s[4:5]
	s_lshl_b32 s4, s18, 4
	s_lshl_b32 s5, s19, 1
	s_or_b32 s4, s5, s4
	s_ashr_i32 s5, s4, 31
	s_lshl_b64 s[4:5], s[4:5], 2
	s_add_u32 s18, s31, s4
	s_addc_u32 s19, s34, s5
	s_add_u32 s4, s88, s4
	s_addc_u32 s5, s89, s5
	global_load_dword v10, v163, s[18:19]
	global_load_dword v11, v199, s[4:5] offset:4
	s_waitcnt vmcnt(0)
	s_waitcnt vmcnt(0) lgkmcnt(0)
	s_barrier
	v_mov_b32_e32 v207, 0
	v_lshlrev_b32_e32 v3, 4, v2
	v_lshlrev_b32_e32 v13, 7, v12
	v_and_b32_e32 v14, 0xf0, v3
	v_lshl_add_u32 v15, v2, 8, s24
	v_xad_u32 v2, v13, v14, v15
	ds_read_b128 v[2:5], v2
	v_or_b32_e32 v6, 16, v13
	v_xad_u32 v6, v6, v14, v15
	ds_read_b128 v[6:9], v6
	v_cmp_eq_u32_e32 vcc, 0, v12
	s_waitcnt lgkmcnt(1)
	v_lshlrev_b32_e32 v16, 16, v2
	v_and_b32_e32 v2, 0xffff0000, v2
	v_mul_f32_e32 v2, v2, v2
	v_fmac_f32_e32 v2, v16, v16
	v_lshlrev_b32_e32 v16, 16, v3
	v_and_b32_e32 v3, 0xffff0000, v3
	v_mul_f32_e32 v3, v3, v3
	v_fmac_f32_e32 v3, v16, v16
	v_add_f32_e32 v2, v2, v3
	v_lshlrev_b32_e32 v3, 16, v4
	v_and_b32_e32 v4, 0xffff0000, v4
	v_mul_f32_e32 v4, v4, v4
	v_fmac_f32_e32 v4, v3, v3
	v_add_f32_e32 v2, v4, v2
	v_and_b32_e32 v4, 0xffff0000, v5
	v_lshlrev_b32_e32 v3, 16, v5
	v_mul_f32_e32 v4, v4, v4
	v_fmac_f32_e32 v4, v3, v3
	v_add_f32_e32 v2, v4, v2
	s_waitcnt lgkmcnt(0)
	v_and_b32_e32 v4, 0xffff0000, v6
	v_lshlrev_b32_e32 v3, 16, v6
	v_mul_f32_e32 v4, v4, v4
	v_fmac_f32_e32 v4, v3, v3
	v_add_f32_e32 v2, v4, v2
	v_and_b32_e32 v4, 0xffff0000, v7
	v_lshlrev_b32_e32 v3, 16, v7
	v_mul_f32_e32 v4, v4, v4
	v_fmac_f32_e32 v4, v3, v3
	v_add_f32_e32 v2, v4, v2
	v_and_b32_e32 v4, 0xffff0000, v8
	v_lshlrev_b32_e32 v3, 16, v8
	v_mul_f32_e32 v4, v4, v4
	v_fmac_f32_e32 v4, v3, v3
	v_and_b32_e32 v3, 0xffff0000, v9
	v_add_f32_e32 v6, v4, v2
	v_lshlrev_b32_e32 v2, 16, v9
	v_mul_f32_e32 v7, v3, v3
	v_fmac_f32_e32 v7, v2, v2
	v_or_b32_e32 v2, 32, v13
	v_xad_u32 v2, v2, v14, v15
	ds_read_b128 v[2:5], v2
	v_add_f32_e32 v16, v7, v6
	v_or_b32_e32 v6, 48, v13
	v_xad_u32 v6, v6, v14, v15
	ds_read_b128 v[6:9], v6
	s_waitcnt lgkmcnt(1)
	v_lshlrev_b32_e32 v17, 16, v2
	v_and_b32_e32 v2, 0xffff0000, v2
	v_mul_f32_e32 v2, v2, v2
	v_fmac_f32_e32 v2, v17, v17
	v_add_f32_e32 v2, v2, v16
	v_lshlrev_b32_e32 v16, 16, v3
	v_and_b32_e32 v3, 0xffff0000, v3
	v_mul_f32_e32 v3, v3, v3
	v_fmac_f32_e32 v3, v16, v16
	v_add_f32_e32 v2, v3, v2
	v_lshlrev_b32_e32 v3, 16, v4
	v_and_b32_e32 v4, 0xffff0000, v4
	v_mul_f32_e32 v4, v4, v4
	v_fmac_f32_e32 v4, v3, v3
	v_add_f32_e32 v2, v4, v2
	v_and_b32_e32 v4, 0xffff0000, v5
	v_lshlrev_b32_e32 v3, 16, v5
	v_mul_f32_e32 v4, v4, v4
	v_fmac_f32_e32 v4, v3, v3
	v_add_f32_e32 v2, v4, v2
	s_waitcnt lgkmcnt(0)
	v_and_b32_e32 v4, 0xffff0000, v6
	v_lshlrev_b32_e32 v3, 16, v6
	v_mul_f32_e32 v4, v4, v4
	v_fmac_f32_e32 v4, v3, v3
	v_add_f32_e32 v2, v4, v2
	v_and_b32_e32 v4, 0xffff0000, v7
	v_lshlrev_b32_e32 v3, 16, v7
	v_mul_f32_e32 v4, v4, v4
	v_fmac_f32_e32 v4, v3, v3
	v_add_f32_e32 v2, v4, v2
	v_and_b32_e32 v4, 0xffff0000, v8
	v_lshlrev_b32_e32 v3, 16, v8
	v_mul_f32_e32 v4, v4, v4
	v_fmac_f32_e32 v4, v3, v3
	v_and_b32_e32 v3, 0xffff0000, v9
	v_add_f32_e32 v6, v4, v2
	v_lshlrev_b32_e32 v2, 16, v9
	v_mul_f32_e32 v7, v3, v3
	v_fmac_f32_e32 v7, v2, v2
	v_or_b32_e32 v2, 64, v13
	v_xad_u32 v2, v2, v14, v15
	ds_read_b128 v[2:5], v2
	v_add_f32_e32 v16, v7, v6
	v_or_b32_e32 v6, 0x50, v13
	v_xad_u32 v6, v6, v14, v15
	ds_read_b128 v[6:9], v6
	s_waitcnt lgkmcnt(1)
	v_lshlrev_b32_e32 v17, 16, v2
	v_and_b32_e32 v2, 0xffff0000, v2
	v_mul_f32_e32 v2, v2, v2
	v_fmac_f32_e32 v2, v17, v17
	v_add_f32_e32 v2, v2, v16
	v_lshlrev_b32_e32 v16, 16, v3
	v_and_b32_e32 v3, 0xffff0000, v3
	v_mul_f32_e32 v3, v3, v3
	v_fmac_f32_e32 v3, v16, v16
	v_add_f32_e32 v2, v3, v2
	v_lshlrev_b32_e32 v3, 16, v4
	v_and_b32_e32 v4, 0xffff0000, v4
	v_mul_f32_e32 v4, v4, v4
	v_fmac_f32_e32 v4, v3, v3
	v_add_f32_e32 v2, v4, v2
	v_and_b32_e32 v4, 0xffff0000, v5
	v_lshlrev_b32_e32 v3, 16, v5
	v_mul_f32_e32 v4, v4, v4
	v_fmac_f32_e32 v4, v3, v3
	v_add_f32_e32 v2, v4, v2
	s_waitcnt lgkmcnt(0)
	v_and_b32_e32 v4, 0xffff0000, v6
	v_lshlrev_b32_e32 v3, 16, v6
	v_mul_f32_e32 v4, v4, v4
	v_fmac_f32_e32 v4, v3, v3
	v_add_f32_e32 v2, v4, v2
	v_and_b32_e32 v4, 0xffff0000, v7
	v_lshlrev_b32_e32 v3, 16, v7
	v_mul_f32_e32 v4, v4, v4
	v_fmac_f32_e32 v4, v3, v3
	v_add_f32_e32 v2, v4, v2
	v_and_b32_e32 v4, 0xffff0000, v8
	v_lshlrev_b32_e32 v3, 16, v8
	v_mul_f32_e32 v4, v4, v4
	v_fmac_f32_e32 v4, v3, v3
	v_and_b32_e32 v3, 0xffff0000, v9
	v_add_f32_e32 v6, v4, v2
	v_lshlrev_b32_e32 v2, 16, v9
	v_mul_f32_e32 v7, v3, v3
	v_fmac_f32_e32 v7, v2, v2
	v_or_b32_e32 v2, 0x60, v13
	v_xad_u32 v2, v2, v14, v15
	ds_read_b128 v[2:5], v2
	v_add_f32_e32 v16, v7, v6
	v_or_b32_e32 v6, 0x70, v13
	v_xad_u32 v6, v6, v14, v15
	ds_read_b128 v[6:9], v6
	s_waitcnt lgkmcnt(1)
	v_lshlrev_b32_e32 v13, 16, v2
	v_and_b32_e32 v2, 0xffff0000, v2
	v_mul_f32_e32 v2, v2, v2
	v_fmac_f32_e32 v2, v13, v13
	v_lshlrev_b32_e32 v13, 16, v3
	v_and_b32_e32 v3, 0xffff0000, v3
	v_mul_f32_e32 v3, v3, v3
	v_add_f32_e32 v2, v2, v16
	v_fmac_f32_e32 v3, v13, v13
	v_add_f32_e32 v2, v3, v2
	v_lshlrev_b32_e32 v3, 16, v4
	v_and_b32_e32 v4, 0xffff0000, v4
	v_mul_f32_e32 v4, v4, v4
	v_fmac_f32_e32 v4, v3, v3
	v_add_f32_e32 v2, v4, v2
	v_and_b32_e32 v4, 0xffff0000, v5
	v_lshlrev_b32_e32 v3, 16, v5
	v_mul_f32_e32 v4, v4, v4
	v_fmac_f32_e32 v4, v3, v3
	v_add_f32_e32 v13, v4, v2
	s_waitcnt lgkmcnt(0)
	v_and_b32_e32 v5, 0xffff0000, v7
	v_and_b32_e32 v4, 0xffff0000, v6
	v_lshlrev_b32_e32 v3, 16, v7
	v_lshlrev_b32_e32 v2, 16, v6
	v_pk_mul_f32 v[4:5], v[4:5], v[4:5]
	v_mov_b32_e32 v206, 0
	v_pk_fma_f32 v[2:3], v[2:3], v[2:3], v[4:5]
	v_and_b32_e32 v5, 0xffff0000, v9
	v_add_f32_e32 v2, v2, v13
	v_and_b32_e32 v4, 0xffff0000, v8
	v_add_f32_e32 v6, v3, v2
	v_lshlrev_b32_e32 v3, 16, v9
	v_lshlrev_b32_e32 v2, 16, v8
	v_pk_mul_f32 v[4:5], v[4:5], v[4:5]
	s_mov_b32 s72, 0
	v_pk_fma_f32 v[2:3], v[2:3], v[2:3], v[4:5]
	v_mov_b32_e32 v7, v163
	v_add_f32_e32 v2, v2, v6
	v_add_f32_e32 v2, v3, v2
	v_cndmask_b32_e32 v3, v11, v10, vcc
	v_mul_f32_e32 v2, v3, v2
	v_mul_f32_e32 v3, 0x4f800000, v2
	v_cmp_gt_f32_e32 vcc, s45, v2
	v_mov_b32_e32 v6, v163
	v_mov_b32_e32 v8, v163
	v_cndmask_b32_e32 v2, v2, v3, vcc
	v_sqrt_f32_e32 v3, v2
	v_mov_b32_e32 v9, v163
	v_mov_b32_e32 v10, v163
	v_mov_b32_e32 v11, v163
	v_add_u32_e32 v4, -1, v3
	v_fma_f32 v5, -v4, v3, v2
	v_cmp_ge_f32_e64 s[4:5], 0, v5
	v_add_u32_e32 v5, 1, v3
	v_mov_b32_e32 v12, v163
	v_cndmask_b32_e64 v4, v3, v4, s[4:5]
	v_fma_f32 v3, -v5, v3, v2
	v_cmp_lt_f32_e64 s[4:5], 0, v3
	v_mov_b32_e32 v13, v163
	v_mov_b32_e32 v14, v163
	v_cndmask_b32_e64 v3, v4, v5, s[4:5]
	v_mul_f32_e32 v4, 0x37800000, v3
	v_cndmask_b32_e32 v3, v3, v4, vcc
	v_cmp_class_f32_e32 vcc, v2, v200
	v_mov_b32_e32 v4, v163
	v_mov_b32_e32 v5, v163
	v_cndmask_b32_e32 v2, v3, v2, vcc
	v_mov_b32_e32 v3, v2
	s_nop 1
	v_permlane32_swap_b32_e32 v2, v3
	v_fmamk_f32 v2, v2, 0x3f8147ae, v201
	v_max_f32_e32 v204, 0, v2
	v_fmamk_f32 v2, v3, 0x3f8147ae, v201
	v_max_f32_e32 v205, 0, v2
	v_cmp_eq_f32_e32 vcc, 0, v204
	v_cmp_eq_f32_e64 s[4:5], 0, v205
	s_and_b64 s[4:5], vcc, s[4:5]
	v_mov_b32_e32 v3, v163
	v_cndmask_b32_e64 v2, 0, 1, s[4:5]
	v_cmp_ne_u32_e32 vcc, 0, v2
	s_cmp_eq_u64 vcc, exec
	s_cselect_b64 s[4:5], -1, 0
	v_cndmask_b32_e64 v2, 0, 1, s[4:5]
	v_mov_b32_e32 v15, v163
	v_readfirstlane_b32 s4, v2
	s_bitcmp1_b32 s4, 0
	s_cselect_b64 s[4:5], -1, 0
	s_xor_b64 s[4:5], s[4:5], -1
	v_cndmask_b32_e64 v208, 0, 1, s[4:5]
	s_addk_i32 s68, 0xff00
	s_or_b32 s69, s65, 0x1400
	v_mov_b32_e32 v2, 0
	v_mov_b32_e32 v16, v163
	v_mov_b32_e32 v17, v163
	v_mov_b32_e32 v18, 0
	v_mov_b32_e32 v19, v163
	v_mov_b32_e32 v20, v163
	v_mov_b32_e32 v21, v163
	v_mov_b32_e32 v22, v163
	v_mov_b32_e32 v23, v163
	v_mov_b32_e32 v24, v163
	v_mov_b32_e32 v25, v163
	v_mov_b32_e32 v26, v163
	v_mov_b32_e32 v27, v163
	v_mov_b32_e32 v28, v163
	v_mov_b32_e32 v29, v163
	v_mov_b32_e32 v30, v163
	v_mov_b32_e32 v31, v163
	v_mov_b32_e32 v32, v163
	v_mov_b32_e32 v33, v163
	v_mov_b32_e32 v34, 0
	v_mov_b32_e32 v35, v163
	v_mov_b32_e32 v36, v163
	v_mov_b32_e32 v37, v163
	v_mov_b32_e32 v38, v163
	v_mov_b32_e32 v39, v163
	v_mov_b32_e32 v40, v163
	v_mov_b32_e32 v41, v163
	v_mov_b32_e32 v42, v163
	v_mov_b32_e32 v43, v163
	v_mov_b32_e32 v44, v163
	v_mov_b32_e32 v45, v163
	v_mov_b32_e32 v46, v163
	v_mov_b32_e32 v47, v163
	v_mov_b32_e32 v48, v163
	v_mov_b32_e32 v49, v163
	v_mov_b32_e32 v50, 0
	v_mov_b32_e32 v51, v163
	v_mov_b32_e32 v52, v163
	v_mov_b32_e32 v53, v163
	v_mov_b32_e32 v54, v163
	v_mov_b32_e32 v55, v163
	v_mov_b32_e32 v56, v163
	v_mov_b32_e32 v57, v163
	v_mov_b32_e32 v58, v163
	v_mov_b32_e32 v59, v163
	v_mov_b32_e32 v60, v163
	v_mov_b32_e32 v61, v163
	v_mov_b32_e32 v62, v163
	v_mov_b32_e32 v63, v163
	v_mov_b32_e32 v64, v163
	v_mov_b32_e32 v65, v163
	v_mov_b32_e32 v82, 0
	v_mov_b32_e32 v83, v163
	v_mov_b32_e32 v84, v163
	v_mov_b32_e32 v85, v163
	v_mov_b32_e32 v86, v163
	v_mov_b32_e32 v87, v163
	v_mov_b32_e32 v88, v163
	v_mov_b32_e32 v89, v163
	v_mov_b32_e32 v90, v163
	v_mov_b32_e32 v91, v163
	v_mov_b32_e32 v92, v163
	v_mov_b32_e32 v93, v163
	v_mov_b32_e32 v94, v163
	v_mov_b32_e32 v95, v163
	v_mov_b32_e32 v96, v163
	v_mov_b32_e32 v97, v163
	v_mov_b32_e32 v66, 0
	v_mov_b32_e32 v67, v163
	v_mov_b32_e32 v68, v163
	v_mov_b32_e32 v69, v163
	v_mov_b32_e32 v70, v163
	v_mov_b32_e32 v71, v163
	v_mov_b32_e32 v72, v163
	v_mov_b32_e32 v73, v163
	v_mov_b32_e32 v74, v163
	v_mov_b32_e32 v75, v163
	v_mov_b32_e32 v76, v163
	v_mov_b32_e32 v77, v163
	v_mov_b32_e32 v78, v163
	v_mov_b32_e32 v79, v163
	v_mov_b32_e32 v80, v163
	v_mov_b32_e32 v81, v163
	v_mov_b32_e32 v98, 0
	v_mov_b32_e32 v99, v163
	v_mov_b32_e32 v100, v163
	v_mov_b32_e32 v101, v163
	v_mov_b32_e32 v102, v163
	v_mov_b32_e32 v103, v163
	v_mov_b32_e32 v104, v163
	v_mov_b32_e32 v105, v163
	v_mov_b32_e32 v106, v163
	v_mov_b32_e32 v107, v163
	v_mov_b32_e32 v108, v163
	v_mov_b32_e32 v109, v163
	v_mov_b32_e32 v110, v163
	v_mov_b32_e32 v111, v163
	v_mov_b32_e32 v112, v163
	v_mov_b32_e32 v113, v163
	v_mov_b32_e32 v114, 0
	v_mov_b32_e32 v115, v163
	v_mov_b32_e32 v116, v163
	v_mov_b32_e32 v117, v163
	v_mov_b32_e32 v118, v163
	v_mov_b32_e32 v119, v163
	v_mov_b32_e32 v120, v163
	v_mov_b32_e32 v121, v163
	v_mov_b32_e32 v122, v163
	v_mov_b32_e32 v123, v163
	v_mov_b32_e32 v124, v163
	v_mov_b32_e32 v125, v163
	v_mov_b32_e32 v126, v163
	v_mov_b32_e32 v127, v163
	v_mov_b32_e32 v128, v163
	v_mov_b32_e32 v129, v163
	v_readfirstlane_b32 s4, v208
	s_nop 3
	s_cmp_lg_u32 s4, 0
	s_cbranch_scc1 .LBB0_640
	s_mul_i32 s4, s79, 0x700
	s_add_i32 s4, s4, 0x20800
	v_lshl_add_u32 v250, v196, 2, s4
	ds_write_b32 v250, v162 offset:0
	ds_write_b32 v250, v164 offset:256
	ds_write_b32 v250, v166 offset:512
	ds_write_b32 v250, v168 offset:768
	ds_write_b32 v250, v170 offset:1024
	ds_write_b32 v250, v172 offset:1280
	ds_write_b32 v250, v174 offset:1536
	v_add_u32_e32 v178, s24, v180
	v_add_u32_e32 v179, s24, v182
	v_add_u32_e32 v181, s24, v184
	v_add_u32_e32 v183, s24, v186
	v_add_u32_e32 v251, s24, v188
	v_add_u32_e32 v255, s24, v194
	v_mov_b32_e32 v130, v196
	v_ashrrev_i32_e32 v131, 4, v130
	v_and_b32_e32 v132, 15, v130
	v_add_u32_e32 v136, s25, v131
	v_bitop3_b32 v137, v136, v132, 15 bitop3:0x6c
	v_mul_lo_u32 v136, v136, s44
	v_ashrrev_i32_e32 v133, 5, v130
	v_add_u32_e32 v136, s67, v136
	v_lshlrev_b32_e32 v137, 4, v137
	v_lshl_or_b32 v136, v136, 1, v137
	v_add_u32_e32 v137, s26, v133
	v_bfe_u32 v134, v130, 2, 3
	v_lshrrev_b32_e32 v135, 1, v130
	v_lshlrev_b32_e32 v138, 1, v137
	v_lshlrev_b32_e32 v135, 3, v130
	v_and_b32_e32 v138, 0xfffff0, v138
	v_and_b32_e32 v137, 4, v137
	v_lshlrev_b32_e32 v137, 1, v137
	v_and_b32_e32 v135, 24, v135
	v_or3_b32 v137, v137, v138, v134
	v_and_b32_e32 v130, 0x60, v130
	v_mul_u32_u24_e32 v137, 0x1900, v137
	v_or3_b32 v130, s69, v130, v135
	v_add_lshl_u32 v130, v130, v137, 1
	v_mov_b32_e32 v185, v136
	v_mov_b32_e32 v187, v130
	v_add_u32_e32 v130, s28, v131
	v_mul_lo_u32 v131, v130, s44
	v_bitop3_b32 v130, v130, v132, 15 bitop3:0x6c
	v_add_u32_e32 v131, s67, v131
	v_lshlrev_b32_e32 v130, 4, v130
	v_lshl_or_b32 v130, v131, 1, v130
	v_mov_b32_e32 v189, v130
	v_add_u32_e32 v131, s29, v133
	v_lshlrev_b32_e32 v132, 1, v131
	v_and_b32_e32 v132, 0xfffff0, v132
	v_and_b32_e32 v133, 4, v131
	v_lshlrev_b32_e32 v133, 1, v133
	v_lshlrev_b32_e32 v131, 5, v131
	v_or3_b32 v132, v133, v132, v134
	v_and_b32_e32 v131, 0x60, v131
	v_mul_u32_u24_e32 v132, 0x1900, v132
	v_or3_b32 v131, s69, v131, v135
	v_add_lshl_u32 v131, v131, v132, 1
	v_mov_b32_e32 v191, v131
	v_mov_b32_e32 v193, 0
	v_mov_b32_e32 v209, 0
	v_mov_b32_e32 v254, v202
	v_add_u32_e32 v250, s24, v190
	ds_read_b128 v[174:177], v250 offset:0
	v_add_u32_e32 v250, s24, v192
	ds_read_b128 v[202:205], v250 offset:0
	s_waitcnt lgkmcnt(0)

.Lfa_skip0:
	s_waitcnt lgkmcnt(10)
	v_mfma_f32_32x32x16_bf16 v[146:161], v[242:245], v[214:217], v[146:161]
	s_waitcnt lgkmcnt(9)
	v_mfma_f32_32x32x16_bf16 v[130:145], v[210:213], v[214:217], v[130:145]
	ds_read_b128 v[242:245], v190 offset:32768
	ds_read_b128 v[246:249], v190 offset:40960
	s_waitcnt lgkmcnt(9)
	v_mfma_f32_32x32x16_bf16 v[146:161], v[218:221], v[226:229], v[146:161]
	s_waitcnt lgkmcnt(8)
	v_mfma_f32_32x32x16_bf16 v[130:145], v[222:225], v[226:229], v[130:145]
	s_waitcnt lgkmcnt(6)
	v_mfma_f32_32x32x16_bf16 v[146:161], v[230:233], v[238:241], v[146:161]
	s_waitcnt lgkmcnt(5)
	v_mfma_f32_32x32x16_bf16 v[130:145], v[234:237], v[238:241], v[130:145]
	s_waitcnt lgkmcnt(3)
	v_mfma_f32_32x32x16_bf16 v[210:225], v[162:165], v[170:173], 0
	s_waitcnt lgkmcnt(2)
	v_mfma_f32_32x32x16_bf16 v[226:241], v[166:169], v[170:173], 0
	ds_read_b128 v[162:165], v192 offset:32768
	ds_read_b128 v[166:169], v192 offset:40960
	s_waitcnt lgkmcnt(3)
	v_mfma_f32_32x32x16_bf16 v[210:225], v[242:245], v[174:177], v[210:225]
	s_nop 1
	v_exp_f32_e32 v146, v146
	v_exp_f32_e32 v147, v147
	v_exp_f32_e32 v148, v148
	v_exp_f32_e32 v149, v149
	v_exp_f32_e32 v150, v150
	s_waitcnt lgkmcnt(2)
	v_mfma_f32_32x32x16_bf16 v[226:241], v[246:249], v[174:177], v[226:241]
	ds_read_b128 v[242:245], v194 offset:32768
	ds_read_b128 v[198:201], v255 offset:0
	ds_read_b128 v[246:249], v194 offset:40960
	v_exp_f32_e32 v151, v151
	v_exp_f32_e32 v152, v152
	v_exp_f32_e32 v153, v153
	v_add_f32_e32 v207, v207, v146
	v_add_f32_e32 v193, v193, v147
	s_waitcnt lgkmcnt(4)
	v_mfma_f32_32x32x16_bf16 v[210:225], v[162:165], v[202:205], v[210:225]
	v_add_f32_e32 v207, v207, v148
	v_add_f32_e32 v193, v193, v149
	v_add_f32_e32 v207, v207, v150
	v_add_f32_e32 v193, v193, v151
	v_add_f32_e32 v207, v207, v152
	s_waitcnt lgkmcnt(3)
	v_mfma_f32_32x32x16_bf16 v[226:241], v[166:169], v[202:205], v[226:241]
	v_add_f32_e32 v193, v193, v153
	v_cvt_pk_bf16_f32 v146, v146, v147
	v_cvt_pk_bf16_f32 v147, v148, v149
	v_cvt_pk_bf16_f32 v148, v150, v151
	v_cvt_pk_bf16_f32 v149, v152, v153
	ds_read_b64_tr_b16 v[162:163], v195 offset:0
	ds_read_b64_tr_b16 v[164:165], v195 offset:2048
	ds_read_b64_tr_b16 v[166:167], v195 offset:512
	ds_read_b64_tr_b16 v[168:169], v195 offset:2560
	ds_read_b64_tr_b16 v[170:171], v195 offset:1024
	ds_read_b64_tr_b16 v[172:173], v195 offset:3072
	s_waitcnt lgkmcnt(7)
	v_mfma_f32_32x32x16_bf16 v[210:225], v[242:245], v[198:201], v[210:225]
	s_waitcnt lgkmcnt(6)
	v_mfma_f32_32x32x16_bf16 v[226:241], v[246:249], v[198:201], v[226:241]
	ds_read_b64_tr_b16 v[242:243], v195 offset:1536
	ds_read_b64_tr_b16 v[244:245], v195 offset:3584
	ds_read_b64_tr_b16 v[246:247], v195 offset:4096
	ds_read_b64_tr_b16 v[248:249], v195 offset:6144
	ds_read_b64_tr_b16 v[198:199], v195 offset:4608
	ds_read_b64_tr_b16 v[200:201], v195 offset:6656
	s_nop 3
	v_exp_f32_e32 v210, v210
	v_exp_f32_e32 v211, v211
	v_exp_f32_e32 v212, v212
	v_exp_f32_e32 v213, v213
	v_exp_f32_e32 v214, v214
	v_exp_f32_e32 v215, v215
	v_exp_f32_e32 v216, v216
	v_exp_f32_e32 v217, v217
	v_add_f32_e32 v206, v206, v210
	v_add_f32_e32 v209, v209, v211
	v_add_f32_e32 v206, v206, v212
	v_add_f32_e32 v209, v209, v213
	v_add_f32_e32 v206, v206, v214
	v_add_f32_e32 v209, v209, v215
	v_add_f32_e32 v206, v206, v216
	v_add_f32_e32 v209, v209, v217
	v_cvt_pk_bf16_f32 v210, v210, v211
	v_cvt_pk_bf16_f32 v211, v212, v213
	v_cvt_pk_bf16_f32 v212, v214, v215
	v_cvt_pk_bf16_f32 v213, v216, v217
	s_waitcnt lgkmcnt(10)
	v_mfma_f32_32x32x16_bf16 v[82:97], v[146:149], v[162:165], v[82:97]
	v_exp_f32_e32 v154, v154
	v_exp_f32_e32 v155, v155
	v_exp_f32_e32 v156, v156
	v_exp_f32_e32 v157, v157
	v_exp_f32_e32 v158, v158
	v_mfma_f32_32x32x16_bf16 v[50:65], v[210:213], v[162:165], v[50:65]
	v_exp_f32_e32 v159, v159
	v_exp_f32_e32 v160, v160
	v_exp_f32_e32 v161, v161
	v_add_f32_e32 v207, v207, v154
	v_add_f32_e32 v193, v193, v155
	ds_read_b64_tr_b16 v[162:163], v195 offset:5120
	ds_read_b64_tr_b16 v[164:165], v195 offset:7168
	s_waitcnt lgkmcnt(10)
	v_mfma_f32_32x32x16_bf16 v[66:81], v[146:149], v[166:169], v[66:81]
	v_add_f32_e32 v207, v207, v156
	v_add_f32_e32 v193, v193, v157
	v_add_f32_e32 v207, v207, v158
	v_add_f32_e32 v193, v193, v159
	v_add_f32_e32 v207, v207, v160
	v_mfma_f32_32x32x16_bf16 v[34:49], v[210:213], v[166:169], v[34:49]
	v_add_f32_e32 v193, v193, v161
	v_cvt_pk_bf16_f32 v154, v154, v155
	v_cvt_pk_bf16_f32 v155, v156, v157
	v_cvt_pk_bf16_f32 v156, v158, v159
	v_cvt_pk_bf16_f32 v157, v160, v161
	ds_read_b64_tr_b16 v[166:167], v195 offset:5632
	ds_read_b64_tr_b16 v[168:169], v195 offset:7680
	s_waitcnt lgkmcnt(10)
	v_mfma_f32_32x32x16_bf16 v[98:113], v[146:149], v[170:173], v[98:113]
	v_exp_f32_e32 v218, v218
	v_exp_f32_e32 v219, v219
	v_exp_f32_e32 v220, v220
	v_exp_f32_e32 v221, v221
	v_exp_f32_e32 v222, v222
	v_mfma_f32_32x32x16_bf16 v[18:33], v[210:213], v[170:173], v[18:33]
	v_exp_f32_e32 v223, v223
	v_exp_f32_e32 v224, v224
	v_exp_f32_e32 v225, v225
	v_add_f32_e32 v206, v206, v218
	v_add_f32_e32 v209, v209, v219
	ds_read_b64_tr_b16 v[170:171], v195 offset:8192
	ds_read_b64_tr_b16 v[172:173], v195 offset:10240
	s_waitcnt lgkmcnt(10)
	v_mfma_f32_32x32x16_bf16 v[114:129], v[146:149], v[242:245], v[114:129]
	v_add_f32_e32 v206, v206, v220
	v_add_f32_e32 v209, v209, v221
	v_add_f32_e32 v206, v206, v222
	v_add_f32_e32 v209, v209, v223
	v_add_f32_e32 v206, v206, v224
	v_mfma_f32_32x32x16_bf16 v[2:17], v[210:213], v[242:245], v[2:17]
	v_add_f32_e32 v209, v209, v225
	v_cvt_pk_bf16_f32 v218, v218, v219
	v_cvt_pk_bf16_f32 v219, v220, v221
	v_cvt_pk_bf16_f32 v220, v222, v223
	v_cvt_pk_bf16_f32 v221, v224, v225
	ds_read_b64_tr_b16 v[242:243], v195 offset:8704
	ds_read_b64_tr_b16 v[244:245], v195 offset:10752
	s_waitcnt lgkmcnt(10)
	v_mfma_f32_32x32x16_bf16 v[82:97], v[154:157], v[246:249], v[82:97]
	v_exp_f32_e32 v130, v130
	v_exp_f32_e32 v131, v131
	v_exp_f32_e32 v132, v132
	v_exp_f32_e32 v133, v133
	v_exp_f32_e32 v134, v134
	v_mfma_f32_32x32x16_bf16 v[50:65], v[218:221], v[246:249], v[50:65]
	v_exp_f32_e32 v135, v135
	v_exp_f32_e32 v136, v136
	v_exp_f32_e32 v137, v137
	v_add_f32_e32 v207, v207, v130
	v_add_f32_e32 v193, v193, v131
	ds_read_b64_tr_b16 v[246:247], v195 offset:9216
	ds_read_b64_tr_b16 v[248:249], v195 offset:11264
	s_waitcnt lgkmcnt(10)
	v_mfma_f32_32x32x16_bf16 v[66:81], v[154:157], v[198:201], v[66:81]
	v_add_f32_e32 v207, v207, v132
	v_add_f32_e32 v193, v193, v133
	v_add_f32_e32 v207, v207, v134
	v_add_f32_e32 v193, v193, v135
	v_add_f32_e32 v207, v207, v136
	v_mfma_f32_32x32x16_bf16 v[34:49], v[218:221], v[198:201], v[34:49]
	v_add_f32_e32 v193, v193, v137
	v_cvt_pk_bf16_f32 v130, v130, v131
	v_cvt_pk_bf16_f32 v131, v132, v133
	v_cvt_pk_bf16_f32 v132, v134, v135
	v_cvt_pk_bf16_f32 v133, v136, v137
	ds_read_b64_tr_b16 v[198:199], v195 offset:9728
	ds_read_b64_tr_b16 v[200:201], v195 offset:11776
	s_waitcnt lgkmcnt(10)
	v_mfma_f32_32x32x16_bf16 v[98:113], v[154:157], v[162:165], v[98:113]
	v_exp_f32_e32 v226, v226
	v_exp_f32_e32 v227, v227
	v_exp_f32_e32 v228, v228
	v_exp_f32_e32 v229, v229
	v_exp_f32_e32 v230, v230
	v_mfma_f32_32x32x16_bf16 v[18:33], v[218:221], v[162:165], v[18:33]
	v_exp_f32_e32 v231, v231
	v_exp_f32_e32 v232, v232
	v_exp_f32_e32 v233, v233
	v_add_f32_e32 v206, v206, v226
	v_add_f32_e32 v209, v209, v227
	ds_read_b64_tr_b16 v[162:163], v195 offset:12288
	ds_read_b64_tr_b16 v[164:165], v195 offset:14336
	s_waitcnt lgkmcnt(10)
	v_mfma_f32_32x32x16_bf16 v[114:129], v[154:157], v[166:169], v[114:129]
	v_add_f32_e32 v206, v206, v228
	v_add_f32_e32 v209, v209, v229
	v_add_f32_e32 v206, v206, v230
	v_add_f32_e32 v209, v209, v231
	v_add_f32_e32 v206, v206, v232
	v_mfma_f32_32x32x16_bf16 v[2:17], v[218:221], v[166:169], v[2:17]
	v_add_f32_e32 v209, v209, v233
	v_cvt_pk_bf16_f32 v226, v226, v227
	v_cvt_pk_bf16_f32 v227, v228, v229
	v_cvt_pk_bf16_f32 v228, v230, v231
	v_cvt_pk_bf16_f32 v229, v232, v233
	ds_read_b64_tr_b16 v[166:167], v195 offset:12800
	ds_read_b64_tr_b16 v[168:169], v195 offset:14848
	s_waitcnt lgkmcnt(10)
	v_mfma_f32_32x32x16_bf16 v[82:97], v[130:133], v[170:173], v[82:97]
	v_exp_f32_e32 v138, v138
	v_exp_f32_e32 v139, v139
	v_exp_f32_e32 v140, v140
	v_exp_f32_e32 v141, v141
	v_exp_f32_e32 v142, v142
	v_mfma_f32_32x32x16_bf16 v[50:65], v[226:229], v[170:173], v[50:65]
	v_exp_f32_e32 v143, v143
	v_exp_f32_e32 v144, v144
	v_exp_f32_e32 v145, v145
	v_add_f32_e32 v207, v207, v138
	v_add_f32_e32 v193, v193, v139
	ds_read_b64_tr_b16 v[170:171], v195 offset:13312
	ds_read_b64_tr_b16 v[172:173], v195 offset:15360
	s_waitcnt lgkmcnt(10)
	v_mfma_f32_32x32x16_bf16 v[66:81], v[130:133], v[242:245], v[66:81]
	v_add_f32_e32 v207, v207, v140
	v_add_f32_e32 v193, v193, v141
	v_add_f32_e32 v207, v207, v142
	v_add_f32_e32 v193, v193, v143
	v_add_f32_e32 v207, v207, v144
	v_mfma_f32_32x32x16_bf16 v[34:49], v[226:229], v[242:245], v[34:49]
	v_add_f32_e32 v193, v193, v145
	v_cvt_pk_bf16_f32 v138, v138, v139
	v_cvt_pk_bf16_f32 v139, v140, v141
	v_cvt_pk_bf16_f32 v140, v142, v143
	v_cvt_pk_bf16_f32 v141, v144, v145
	ds_read_b64_tr_b16 v[242:243], v195 offset:13824
	ds_read_b64_tr_b16 v[244:245], v195 offset:15872
	s_waitcnt lgkmcnt(10)
	v_mfma_f32_32x32x16_bf16 v[98:113], v[130:133], v[246:249], v[98:113]
	v_exp_f32_e32 v234, v234
	v_exp_f32_e32 v235, v235
	v_exp_f32_e32 v236, v236
	v_exp_f32_e32 v237, v237
	v_exp_f32_e32 v238, v238
	v_mfma_f32_32x32x16_bf16 v[18:33], v[226:229], v[246:249], v[18:33]
	v_exp_f32_e32 v239, v239
	v_exp_f32_e32 v240, v240
	v_exp_f32_e32 v241, v241
	v_add_f32_e32 v206, v206, v234
	v_add_f32_e32 v209, v209, v235
	s_waitcnt lgkmcnt(8)
	v_mfma_f32_32x32x16_bf16 v[114:129], v[130:133], v[198:201], v[114:129]
	v_add_f32_e32 v206, v206, v236
	v_add_f32_e32 v209, v209, v237
	v_add_f32_e32 v206, v206, v238
	v_add_f32_e32 v209, v209, v239
	v_add_f32_e32 v206, v206, v240
	v_mfma_f32_32x32x16_bf16 v[2:17], v[226:229], v[198:201], v[2:17]
	v_add_f32_e32 v209, v209, v241
	v_cvt_pk_bf16_f32 v234, v234, v235
	v_cvt_pk_bf16_f32 v235, v236, v237
	v_cvt_pk_bf16_f32 v236, v238, v239
	v_cvt_pk_bf16_f32 v237, v240, v241
	s_waitcnt lgkmcnt(6)
	v_mfma_f32_32x32x16_bf16 v[82:97], v[138:141], v[162:165], v[82:97]
	v_mfma_f32_32x32x16_bf16 v[50:65], v[234:237], v[162:165], v[50:65]
	s_waitcnt lgkmcnt(4)
	v_mfma_f32_32x32x16_bf16 v[66:81], v[138:141], v[166:169], v[66:81]
	v_mfma_f32_32x32x16_bf16 v[34:49], v[234:237], v[166:169], v[34:49]
	s_waitcnt lgkmcnt(2)
	v_mfma_f32_32x32x16_bf16 v[98:113], v[138:141], v[170:173], v[98:113]
	v_mfma_f32_32x32x16_bf16 v[18:33], v[234:237], v[170:173], v[18:33]
	s_waitcnt lgkmcnt(0)
	v_mfma_f32_32x32x16_bf16 v[114:129], v[138:141], v[242:245], v[114:129]
	v_mfma_f32_32x32x16_bf16 v[2:17], v[234:237], v[242:245], v[2:17]
	s_add_i32 s72, s72, 1
	s_add_i32 s71, s71, 64
	s_addk_i32 s70, 0x4000
	s_waitcnt vmcnt(0)
	s_barrier
	ds_read_b128 v[162:165], v180 offset:49152
	ds_read_b128 v[170:173], v178 offset:0
	ds_read_b128 v[166:169], v180 offset:57344
	ds_read_b128 v[242:245], v182 offset:49152
	ds_read_b128 v[214:217], v179 offset:0
	ds_read_b128 v[210:213], v182 offset:57344
	ds_read_b128 v[218:221], v184 offset:49152
	ds_read_b128 v[226:229], v181 offset:0
	ds_read_b128 v[222:225], v184 offset:57344
	ds_read_b128 v[230:233], v186 offset:49152
	ds_read_b128 v[238:241], v183 offset:0
	ds_read_b128 v[234:237], v186 offset:57344
	s_waitcnt lgkmcnt(10)
	v_mfma_f32_32x32x16_bf16 v[146:161], v[162:165], v[170:173], 0
	s_waitcnt lgkmcnt(9)
	v_mfma_f32_32x32x16_bf16 v[130:145], v[166:169], v[170:173], 0
	ds_read_b128 v[162:165], v188 offset:49152
	ds_read_b128 v[170:173], v251 offset:0
	ds_read_b128 v[166:169], v188 offset:57344
	s_cmpk_eq_i32 s72, 0x43
	s_cbranch_scc1 .Lfa_skip1
	s_cmp_lt_u32 s72, 3
	s_cselect_b32 s5, s66, s68
	s_add_i32 s5, s5, s71
	s_mul_hi_i32 s19, s5, 0x3200
	s_mulk_i32 s5, 0x3200
	s_add_u32 s18, s20, s5
	s_addc_u32 s19, s21, s19
	s_add_i32 s75, s27, 0x0
	s_add_i32 s5, s30, 0x0
	s_add_i32 m0, s75, 0x8000
	s_nop 0
	global_load_lds_dwordx4 v185, s[18:19]
	s_mov_b32 m0, s75
	s_nop 0
	global_load_lds_dwordx4 v187, s[18:19]
	s_add_i32 m0, s5, 0x8000
	s_nop 0
	global_load_lds_dwordx4 v189, s[18:19]
	s_mov_b32 m0, s5
	s_nop 0
	global_load_lds_dwordx4 v191, s[18:19]
.Lfa_skip1:
	s_waitcnt lgkmcnt(10)
	v_mfma_f32_32x32x16_bf16 v[146:161], v[242:245], v[214:217], v[146:161]
	s_waitcnt lgkmcnt(9)
	v_mfma_f32_32x32x16_bf16 v[130:145], v[210:213], v[214:217], v[130:145]
	ds_read_b128 v[242:245], v190 offset:49152
	ds_read_b128 v[246:249], v190 offset:57344
	s_waitcnt lgkmcnt(9)
	v_mfma_f32_32x32x16_bf16 v[146:161], v[218:221], v[226:229], v[146:161]
	s_waitcnt lgkmcnt(8)
	v_mfma_f32_32x32x16_bf16 v[130:145], v[222:225], v[226:229], v[130:145]
	s_waitcnt lgkmcnt(6)
	v_mfma_f32_32x32x16_bf16 v[146:161], v[230:233], v[238:241], v[146:161]
	s_waitcnt lgkmcnt(5)
	v_mfma_f32_32x32x16_bf16 v[130:145], v[234:237], v[238:241], v[130:145]
	s_waitcnt lgkmcnt(3)
	v_mfma_f32_32x32x16_bf16 v[210:225], v[162:165], v[170:173], 0
	s_waitcnt lgkmcnt(2)
	v_mfma_f32_32x32x16_bf16 v[226:241], v[166:169], v[170:173], 0
	ds_read_b128 v[162:165], v192 offset:49152
	ds_read_b128 v[166:169], v192 offset:57344
	s_waitcnt lgkmcnt(3)
	v_mfma_f32_32x32x16_bf16 v[210:225], v[242:245], v[174:177], v[210:225]
	s_nop 1
	v_exp_f32_e32 v146, v146
	v_exp_f32_e32 v147, v147
	v_exp_f32_e32 v148, v148
	v_exp_f32_e32 v149, v149
	v_exp_f32_e32 v150, v150
	s_waitcnt lgkmcnt(2)
	v_mfma_f32_32x32x16_bf16 v[226:241], v[246:249], v[174:177], v[226:241]
	ds_read_b128 v[242:245], v194 offset:49152
	ds_read_b128 v[198:201], v255 offset:0
	ds_read_b128 v[246:249], v194 offset:57344
	v_exp_f32_e32 v151, v151
	v_exp_f32_e32 v152, v152
	v_exp_f32_e32 v153, v153
	v_add_f32_e32 v207, v207, v146
	v_add_f32_e32 v193, v193, v147
	s_waitcnt lgkmcnt(4)
	v_mfma_f32_32x32x16_bf16 v[210:225], v[162:165], v[202:205], v[210:225]
	v_add_f32_e32 v207, v207, v148
	v_add_f32_e32 v193, v193, v149
	v_add_f32_e32 v207, v207, v150
	v_add_f32_e32 v193, v193, v151
	v_add_f32_e32 v207, v207, v152
	s_waitcnt lgkmcnt(3)
	v_mfma_f32_32x32x16_bf16 v[226:241], v[166:169], v[202:205], v[226:241]
	v_add_f32_e32 v193, v193, v153
	v_cvt_pk_bf16_f32 v146, v146, v147
	v_cvt_pk_bf16_f32 v147, v148, v149
	v_cvt_pk_bf16_f32 v148, v150, v151
	v_cvt_pk_bf16_f32 v149, v152, v153
	ds_read_b64_tr_b16 v[162:163], v195 offset:16384
	ds_read_b64_tr_b16 v[164:165], v195 offset:18432
	ds_read_b64_tr_b16 v[166:167], v195 offset:16896
	ds_read_b64_tr_b16 v[168:169], v195 offset:18944
	ds_read_b64_tr_b16 v[170:171], v195 offset:17408
	ds_read_b64_tr_b16 v[172:173], v195 offset:19456
	s_waitcnt lgkmcnt(7)
	v_mfma_f32_32x32x16_bf16 v[210:225], v[242:245], v[198:201], v[210:225]
	s_waitcnt lgkmcnt(6)
	v_mfma_f32_32x32x16_bf16 v[226:241], v[246:249], v[198:201], v[226:241]
	ds_read_b64_tr_b16 v[242:243], v195 offset:17920
	ds_read_b64_tr_b16 v[244:245], v195 offset:19968
	ds_read_b64_tr_b16 v[246:247], v195 offset:20480
	ds_read_b64_tr_b16 v[248:249], v195 offset:22528
	ds_read_b64_tr_b16 v[198:199], v195 offset:20992
	ds_read_b64_tr_b16 v[200:201], v195 offset:23040
	s_nop 3
	v_exp_f32_e32 v210, v210
	v_exp_f32_e32 v211, v211
	v_exp_f32_e32 v212, v212
	v_exp_f32_e32 v213, v213
	v_exp_f32_e32 v214, v214
	v_exp_f32_e32 v215, v215
	v_exp_f32_e32 v216, v216
	v_exp_f32_e32 v217, v217
	v_add_f32_e32 v206, v206, v210
	v_add_f32_e32 v209, v209, v211
	v_add_f32_e32 v206, v206, v212
	v_add_f32_e32 v209, v209, v213
	v_add_f32_e32 v206, v206, v214
	v_add_f32_e32 v209, v209, v215
	v_add_f32_e32 v206, v206, v216
	v_add_f32_e32 v209, v209, v217
	v_cvt_pk_bf16_f32 v210, v210, v211
	v_cvt_pk_bf16_f32 v211, v212, v213
	v_cvt_pk_bf16_f32 v212, v214, v215
	v_cvt_pk_bf16_f32 v213, v216, v217
	s_waitcnt lgkmcnt(10)
	v_mfma_f32_32x32x16_bf16 v[82:97], v[146:149], v[162:165], v[82:97]
	v_exp_f32_e32 v154, v154
	v_exp_f32_e32 v155, v155
	v_exp_f32_e32 v156, v156
	v_exp_f32_e32 v157, v157
	v_exp_f32_e32 v158, v158
	v_mfma_f32_32x32x16_bf16 v[50:65], v[210:213], v[162:165], v[50:65]
	v_exp_f32_e32 v159, v159
	v_exp_f32_e32 v160, v160
	v_exp_f32_e32 v161, v161
	v_add_f32_e32 v207, v207, v154
	v_add_f32_e32 v193, v193, v155
	ds_read_b64_tr_b16 v[162:163], v195 offset:21504
	ds_read_b64_tr_b16 v[164:165], v195 offset:23552
	s_waitcnt lgkmcnt(10)
	v_mfma_f32_32x32x16_bf16 v[66:81], v[146:149], v[166:169], v[66:81]
	v_add_f32_e32 v207, v207, v156
	v_add_f32_e32 v193, v193, v157
	v_add_f32_e32 v207, v207, v158
	v_add_f32_e32 v193, v193, v159
	v_add_f32_e32 v207, v207, v160
	v_mfma_f32_32x32x16_bf16 v[34:49], v[210:213], v[166:169], v[34:49]
	v_add_f32_e32 v193, v193, v161
	v_cvt_pk_bf16_f32 v154, v154, v155
	v_cvt_pk_bf16_f32 v155, v156, v157
	v_cvt_pk_bf16_f32 v156, v158, v159
	v_cvt_pk_bf16_f32 v157, v160, v161
	ds_read_b64_tr_b16 v[166:167], v195 offset:22016
	ds_read_b64_tr_b16 v[168:169], v195 offset:24064
	s_waitcnt lgkmcnt(10)
	v_mfma_f32_32x32x16_bf16 v[98:113], v[146:149], v[170:173], v[98:113]
	v_exp_f32_e32 v218, v218
	v_exp_f32_e32 v219, v219
	v_exp_f32_e32 v220, v220
	v_exp_f32_e32 v221, v221
	v_exp_f32_e32 v222, v222
	v_mfma_f32_32x32x16_bf16 v[18:33], v[210:213], v[170:173], v[18:33]
	v_exp_f32_e32 v223, v223
	v_exp_f32_e32 v224, v224
	v_exp_f32_e32 v225, v225
	v_add_f32_e32 v206, v206, v218
	v_add_f32_e32 v209, v209, v219
	ds_read_b64_tr_b16 v[170:171], v195 offset:24576
	ds_read_b64_tr_b16 v[172:173], v195 offset:26624
	s_waitcnt lgkmcnt(10)
	v_mfma_f32_32x32x16_bf16 v[114:129], v[146:149], v[242:245], v[114:129]
	v_add_f32_e32 v206, v206, v220
	v_add_f32_e32 v209, v209, v221
	v_add_f32_e32 v206, v206, v222
	v_add_f32_e32 v209, v209, v223
	v_add_f32_e32 v206, v206, v224
	v_mfma_f32_32x32x16_bf16 v[2:17], v[210:213], v[242:245], v[2:17]
	v_add_f32_e32 v209, v209, v225
	v_cvt_pk_bf16_f32 v218, v218, v219
	v_cvt_pk_bf16_f32 v219, v220, v221
	v_cvt_pk_bf16_f32 v220, v222, v223
	v_cvt_pk_bf16_f32 v221, v224, v225
	ds_read_b64_tr_b16 v[242:243], v195 offset:25088
	ds_read_b64_tr_b16 v[244:245], v195 offset:27136
	s_waitcnt lgkmcnt(10)
	v_mfma_f32_32x32x16_bf16 v[82:97], v[154:157], v[246:249], v[82:97]
	v_exp_f32_e32 v130, v130
	v_exp_f32_e32 v131, v131
	v_exp_f32_e32 v132, v132
	v_exp_f32_e32 v133, v133
	v_exp_f32_e32 v134, v134
	v_mfma_f32_32x32x16_bf16 v[50:65], v[218:221], v[246:249], v[50:65]
	v_exp_f32_e32 v135, v135
	v_exp_f32_e32 v136, v136
	v_exp_f32_e32 v137, v137
	v_add_f32_e32 v207, v207, v130
	v_add_f32_e32 v193, v193, v131
	ds_read_b64_tr_b16 v[246:247], v195 offset:25600
	ds_read_b64_tr_b16 v[248:249], v195 offset:27648
	s_waitcnt lgkmcnt(10)
	v_mfma_f32_32x32x16_bf16 v[66:81], v[154:157], v[198:201], v[66:81]
	v_add_f32_e32 v207, v207, v132
	v_add_f32_e32 v193, v193, v133
	v_add_f32_e32 v207, v207, v134
	v_add_f32_e32 v193, v193, v135
	v_add_f32_e32 v207, v207, v136
	v_mfma_f32_32x32x16_bf16 v[34:49], v[218:221], v[198:201], v[34:49]
	v_add_f32_e32 v193, v193, v137
	v_cvt_pk_bf16_f32 v130, v130, v131
	v_cvt_pk_bf16_f32 v131, v132, v133
	v_cvt_pk_bf16_f32 v132, v134, v135
	v_cvt_pk_bf16_f32 v133, v136, v137
	ds_read_b64_tr_b16 v[198:199], v195 offset:26112
	ds_read_b64_tr_b16 v[200:201], v195 offset:28160
	s_waitcnt lgkmcnt(10)
	v_mfma_f32_32x32x16_bf16 v[98:113], v[154:157], v[162:165], v[98:113]
	v_exp_f32_e32 v226, v226
	v_exp_f32_e32 v227, v227
	v_exp_f32_e32 v228, v228
	v_exp_f32_e32 v229, v229
	v_exp_f32_e32 v230, v230
	v_mfma_f32_32x32x16_bf16 v[18:33], v[218:221], v[162:165], v[18:33]
	v_exp_f32_e32 v231, v231
	v_exp_f32_e32 v232, v232
	v_exp_f32_e32 v233, v233
	v_add_f32_e32 v206, v206, v226
	v_add_f32_e32 v209, v209, v227
	ds_read_b64_tr_b16 v[162:163], v195 offset:28672
	ds_read_b64_tr_b16 v[164:165], v195 offset:30720
	s_waitcnt lgkmcnt(10)
	v_mfma_f32_32x32x16_bf16 v[114:129], v[154:157], v[166:169], v[114:129]
	v_add_f32_e32 v206, v206, v228
	v_add_f32_e32 v209, v209, v229
	v_add_f32_e32 v206, v206, v230
	v_add_f32_e32 v209, v209, v231
	v_add_f32_e32 v206, v206, v232
	v_mfma_f32_32x32x16_bf16 v[2:17], v[218:221], v[166:169], v[2:17]
	v_add_f32_e32 v209, v209, v233
	v_cvt_pk_bf16_f32 v226, v226, v227
	v_cvt_pk_bf16_f32 v227, v228, v229
	v_cvt_pk_bf16_f32 v228, v230, v231
	v_cvt_pk_bf16_f32 v229, v232, v233
	ds_read_b64_tr_b16 v[166:167], v195 offset:29184
	ds_read_b64_tr_b16 v[168:169], v195 offset:31232
	s_waitcnt lgkmcnt(10)
	v_mfma_f32_32x32x16_bf16 v[82:97], v[130:133], v[170:173], v[82:97]
	v_exp_f32_e32 v138, v138
	v_exp_f32_e32 v139, v139
	v_exp_f32_e32 v140, v140
	v_exp_f32_e32 v141, v141
	v_exp_f32_e32 v142, v142
	v_mfma_f32_32x32x16_bf16 v[50:65], v[226:229], v[170:173], v[50:65]
	v_exp_f32_e32 v143, v143
	v_exp_f32_e32 v144, v144
	v_exp_f32_e32 v145, v145
	v_add_f32_e32 v207, v207, v138
	v_add_f32_e32 v193, v193, v139
	ds_read_b64_tr_b16 v[170:171], v195 offset:29696
	ds_read_b64_tr_b16 v[172:173], v195 offset:31744
	s_waitcnt lgkmcnt(10)
	v_mfma_f32_32x32x16_bf16 v[66:81], v[130:133], v[242:245], v[66:81]
	v_add_f32_e32 v207, v207, v140
	v_add_f32_e32 v193, v193, v141
	v_add_f32_e32 v207, v207, v142
	v_add_f32_e32 v193, v193, v143
	v_add_f32_e32 v207, v207, v144
	v_mfma_f32_32x32x16_bf16 v[34:49], v[226:229], v[242:245], v[34:49]
	v_add_f32_e32 v193, v193, v145
	v_cvt_pk_bf16_f32 v138, v138, v139
	v_cvt_pk_bf16_f32 v139, v140, v141
	v_cvt_pk_bf16_f32 v140, v142, v143
	v_cvt_pk_bf16_f32 v141, v144, v145
	ds_read_b64_tr_b16 v[242:243], v195 offset:30208
	ds_read_b64_tr_b16 v[244:245], v195 offset:32256
	s_waitcnt lgkmcnt(10)
	v_mfma_f32_32x32x16_bf16 v[98:113], v[130:133], v[246:249], v[98:113]
	v_exp_f32_e32 v234, v234
	v_exp_f32_e32 v235, v235
	v_exp_f32_e32 v236, v236
	v_exp_f32_e32 v237, v237
	v_exp_f32_e32 v238, v238
	v_mfma_f32_32x32x16_bf16 v[18:33], v[226:229], v[246:249], v[18:33]
	v_exp_f32_e32 v239, v239
	v_exp_f32_e32 v240, v240
	v_exp_f32_e32 v241, v241
	v_add_f32_e32 v206, v206, v234
	v_add_f32_e32 v209, v209, v235
	s_waitcnt lgkmcnt(8)
	v_mfma_f32_32x32x16_bf16 v[114:129], v[130:133], v[198:201], v[114:129]
	v_add_f32_e32 v206, v206, v236
	v_add_f32_e32 v209, v209, v237
	v_add_f32_e32 v206, v206, v238
	v_add_f32_e32 v209, v209, v239
	v_add_f32_e32 v206, v206, v240
	v_mfma_f32_32x32x16_bf16 v[2:17], v[226:229], v[198:201], v[2:17]
	v_add_f32_e32 v209, v209, v241
	v_cvt_pk_bf16_f32 v234, v234, v235
	v_cvt_pk_bf16_f32 v235, v236, v237
	v_cvt_pk_bf16_f32 v236, v238, v239
	v_cvt_pk_bf16_f32 v237, v240, v241
	s_waitcnt lgkmcnt(6)
	v_mfma_f32_32x32x16_bf16 v[82:97], v[138:141], v[162:165], v[82:97]
	v_mfma_f32_32x32x16_bf16 v[50:65], v[234:237], v[162:165], v[50:65]
	s_waitcnt lgkmcnt(4)
	v_mfma_f32_32x32x16_bf16 v[66:81], v[138:141], v[166:169], v[66:81]
	v_mfma_f32_32x32x16_bf16 v[34:49], v[234:237], v[166:169], v[34:49]
	s_waitcnt lgkmcnt(2)
	v_mfma_f32_32x32x16_bf16 v[98:113], v[138:141], v[170:173], v[98:113]
	v_mfma_f32_32x32x16_bf16 v[18:33], v[234:237], v[170:173], v[18:33]
	s_waitcnt lgkmcnt(0)
	v_mfma_f32_32x32x16_bf16 v[114:129], v[138:141], v[242:245], v[114:129]
	v_mfma_f32_32x32x16_bf16 v[2:17], v[234:237], v[242:245], v[2:17]
	s_add_i32 s72, s72, 1
	s_add_i32 s71, s71, 64
	s_addk_i32 s70, 0x4000
	s_cmpk_eq_i32 s72, 0x44
	s_waitcnt vmcnt(0)
	s_barrier
	s_cbranch_scc0 .Lfa_loop
	v_add_f32_e32 v207, v207, v193
	v_add_f32_e32 v206, v206, v209
	s_mul_i32 s4, s79, 0x700
	s_add_i32 s4, s4, 0x20800
	v_lshl_add_u32 v250, v196, 2, s4
	ds_read_b32 v162, v250 offset:0
	ds_read_b32 v164, v250 offset:256
	ds_read_b32 v166, v250 offset:512
	ds_read_b32 v168, v250 offset:768
	ds_read_b32 v170, v250 offset:1024
	ds_read_b32 v172, v250 offset:1280
	ds_read_b32 v174, v250 offset:1536
	v_mov_b32_e32 v163, 0
	v_mov_b32_e32 v165, 0
	v_mov_b32_e32 v167, 0
	v_mov_b32_e32 v169, 0
	v_mov_b32_e32 v171, 0
	v_mov_b32_e32 v173, 0
	v_mov_b32_e32 v175, 0
	v_and_b32_e32 v176, 31, v0
	v_lshrrev_b32_e32 v177, 5, v196
	v_mov_b32_e32 v202, v254
	v_lshlrev_b32_e32 v178, 8, v176
	v_mov_b32_e32 v198, 0x2800
	v_mov_b32_e32 v199, 0x8000
	v_mov_b32_e32 v200, 0x260
	v_mov_b32_e32 v201, 0xc2700000
	v_sub_u32_e32 v179, v180, v178
	v_sub_u32_e32 v181, v182, v178
	v_sub_u32_e32 v183, v184, v178
	v_sub_u32_e32 v185, v186, v178
	v_sub_u32_e32 v187, v188, v178
	v_sub_u32_e32 v189, v190, v178
	v_sub_u32_e32 v191, v192, v178
	v_sub_u32_e32 v193, v194, v178
	v_mov_b32_e32 v203, 0x358637bd
	s_waitcnt lgkmcnt(0)
	s_branch .LBB0_651

	.amdhsa_kernel _Z6mk_fwd4Args
		.amdhsa_group_segment_fixed_size 0
		.amdhsa_private_segment_fixed_size 0
		.amdhsa_kernarg_size 448
		.amdhsa_user_sgpr_count 2
		.amdhsa_user_sgpr_dispatch_ptr 0
		.amdhsa_user_sgpr_queue_ptr 0
		.amdhsa_user_sgpr_kernarg_segment_ptr 1
		.amdhsa_user_sgpr_dispatch_id 0
		.amdhsa_user_sgpr_kernarg_preload_length 0
		.amdhsa_user_sgpr_kernarg_preload_offset 0
		.amdhsa_user_sgpr_private_segment_size 0
		.amdhsa_uses_dynamic_stack 0
		.amdhsa_enable_private_segment 0
		.amdhsa_system_sgpr_workgroup_id_x 1
		.amdhsa_system_sgpr_workgroup_id_y 0
		.amdhsa_system_sgpr_workgroup_id_z 0
		.amdhsa_system_sgpr_workgroup_info 0
		.amdhsa_system_vgpr_workitem_id 0
		.amdhsa_next_free_vgpr 256
		.amdhsa_next_free_sgpr 98
		.amdhsa_accum_offset 256
		.amdhsa_reserve_vcc 1
		.amdhsa_float_round_mode_32 0
		.amdhsa_float_round_mode_16_64 0
		.amdhsa_float_denorm_mode_32 3
		.amdhsa_float_denorm_mode_16_64 3
		.amdhsa_dx10_clamp 1
		.amdhsa_ieee_mode 1
		.amdhsa_fp16_overflow 0
		.amdhsa_tg_split 0
		.amdhsa_exception_fp_ieee_invalid_op 0
		.amdhsa_exception_fp_denorm_src 0
		.amdhsa_exception_fp_ieee_div_zero 0
		.amdhsa_exception_fp_ieee_overflow 0
		.amdhsa_exception_fp_ieee_underflow 0
		.amdhsa_exception_fp_ieee_inexact 0
		.amdhsa_exception_int_div_zero 0
	.end_amdhsa_kernel

amdhsa.kernels:
  - .agpr_count:     0
    .args:
      - .offset:         0
        .size:           192
        .value_kind:     by_value
      - .offset:         192
        .size:           4
        .value_kind:     hidden_block_count_x
      - .offset:         196
        .size:           4
        .value_kind:     hidden_block_count_y
      - .offset:         200
        .size:           4
        .value_kind:     hidden_block_count_z
      - .offset:         204
        .size:           2
        .value_kind:     hidden_group_size_x
      - .offset:         206
        .size:           2
        .value_kind:     hidden_group_size_y
      - .offset:         208
        .size:           2
        .value_kind:     hidden_group_size_z
      - .offset:         210
        .size:           2
        .value_kind:     hidden_remainder_x
      - .offset:         212
        .size:           2
        .value_kind:     hidden_remainder_y
      - .offset:         214
        .size:           2
        .value_kind:     hidden_remainder_z
      - .offset:         232
        .size:           8
        .value_kind:     hidden_global_offset_x
      - .offset:         240
        .size:           8
        .value_kind:     hidden_global_offset_y
      - .offset:         248
        .size:           8
        .value_kind:     hidden_global_offset_z
      - .offset:         256
        .size:           2
        .value_kind:     hidden_grid_dims
      - .offset:         312
        .size:           4
        .value_kind:     hidden_dynamic_lds_size
    .group_segment_fixed_size: 0
    .kernarg_segment_align: 8
    .kernarg_segment_size: 448
    .language:       OpenCL C
    .language_version:
      - 2
      - 0
    .max_flat_workgroup_size: 512
    .name:           _Z6mk_fwd4Args
    .private_segment_fixed_size: 0
    .sgpr_count:     104
    .sgpr_spill_count: 77
    .symbol:         _Z6mk_fwd4Args.kd
    .uniform_work_group_size: 1
    .uses_dynamic_stack: false
    .vgpr_count:     256
    .vgpr_spill_count: 0
    .wavefront_size: 64
